# speedup vs baseline: 1.0066x; 1.0033x over previous
.LBB2_5:
	ds_read_b128 v[102:105], v114 offset:8192
	ds_read_b128 v[106:109], v114 offset:10240
	ds_read_b128 v[110:113], v114 offset:12288
	v_exp_f32_e32 v69, v46
	v_exp_f32_e32 v71, v47
	v_exp_f32_e32 v73, v48
	v_exp_f32_e32 v75, v49
	ds_read_b128 v[46:49], v114 offset:14336
	v_exp_f32_e32 v42, v42
	v_exp_f32_e32 v43, v43
	v_exp_f32_e32 v44, v44
	v_exp_f32_e32 v45, v45
	v_cvt_pk_f16_f32 v76, v69, v71
	v_cvt_pk_f16_f32 v77, v73, v75
	v_cvt_pk_f16_f32 v78, v42, v43
	v_cvt_pk_f16_f32 v79, v44, v45
	ds_read_b128 v[42:45], v115 offset:8192
	v_exp_f32_e32 v38, v38
	v_exp_f32_e32 v39, v39
	s_waitcnt lgkmcnt(4)
	v_mfma_f32_16x16x32_f16 v[26:29], v[102:105], v[76:79], v[26:29]
	v_exp_f32_e32 v40, v40
	v_exp_f32_e32 v41, v41
	s_waitcnt lgkmcnt(3)
	v_mfma_f32_16x16x32_f16 v[22:25], v[106:109], v[76:79], v[22:25]
	ds_read_b128 v[102:105], v115 offset:10240
	v_exp_f32_e32 v34, v34
	v_exp_f32_e32 v35, v35
	s_waitcnt lgkmcnt(3)
	v_mfma_f32_16x16x32_f16 v[18:21], v[110:113], v[76:79], v[18:21]
	ds_read_b128 v[106:109], v115 offset:12288
	v_exp_f32_e32 v36, v36
	v_exp_f32_e32 v37, v37
	s_waitcnt lgkmcnt(3)
	v_mfma_f32_16x16x32_f16 v[10:13], v[46:49], v[76:79], v[10:13]
	ds_read_b128 v[110:113], v115 offset:14336
	v_mfma_f32_16x16x32_f16 v[14:17], v[116:119], v[76:79], v[14:17]
	v_cvt_pk_f16_f32 v37, v36, v37
	v_cvt_pk_f16_f32 v36, v34, v35
	v_cvt_pk_f16_f32 v35, v40, v41
	v_cvt_pk_f16_f32 v34, v38, v39
	s_mov_b64 s[38:39], 0
	s_waitcnt lgkmcnt(3)
	v_mfma_f32_16x16x32_f16 v[26:29], v[42:45], v[34:37], v[26:29]
	s_waitcnt lgkmcnt(2)
	v_mfma_f32_16x16x32_f16 v[22:25], v[102:105], v[34:37], v[22:25]
	s_waitcnt lgkmcnt(1)
	v_mfma_f32_16x16x32_f16 v[18:21], v[106:109], v[34:37], v[18:21]
	s_waitcnt lgkmcnt(0)
	v_mfma_f32_16x16x32_f16 v[10:13], v[110:113], v[34:37], v[10:13]
	v_mfma_f32_16x16x32_f16 v[14:17], v[116:119], v[34:37], v[14:17]
